# expert unit scheduler: per-unit panel->expert lookup by scalar load instead of vector load + full vmcnt drain (P11, P12); plus P11 packed epilogue
# speedup vs baseline: 1.0103x; 1.0025x over previous
.LBB0_1406:
	s_andn2_b64 vcc, exec, s[18:19]
	s_cbranch_vccnz .LBB0_1408
	s_ashr_i32 s2, s4, 31
	s_lshr_b32 s2, s2, 29
	s_add_i32 s2, s4, s2
	s_ashr_i32 s5, s2, 3
	s_and_b32 s2, s2, -8
	s_sub_i32 s2, s4, s2
	s_cmp_lt_i32 s2, 0
	s_cselect_b32 s4, s46, s45
	s_mul_i32 s2, s4, s2
	s_add_i32 s2, s2, s5
	s_mul_hi_i32 s4, s2, 0x92492493
	s_add_i32 s4, s4, s2
	s_lshr_b32 s5, s4, 31
	s_ashr_i32 s4, s4, 8
	s_add_i32 s4, s4, s5
	s_lshl_b32 s5, s4, 3
	s_sub_i32 s14, s38, s5
	s_min_i32 s15, s14, 8
	s_abs_i32 s14, s15
	v_cvt_f32_u32_e32 v0, s14
	s_sub_i32 s17, 0, s14
	s_mulk_i32 s4, 0x1c0
	s_sub_i32 s2, s2, s4
	v_rcp_iflag_f32_e32 v0, v0
	s_abs_i32 s4, s2
	s_xor_b32 s16, s2, s15
	s_ashr_i32 s16, s16, 31
	v_mul_f32_e32 v0, 0x4f7ffffe, v0
	v_cvt_u32_f32_e32 v0, v0
	s_nop 0
	v_readfirstlane_b32 s18, v0
	s_mul_i32 s17, s17, s18
	s_mul_hi_u32 s17, s18, s17
	s_add_i32 s18, s18, s17
	s_mul_hi_u32 s17, s4, s18
	s_mul_i32 s18, s17, s14
	s_sub_i32 s4, s4, s18
	s_add_i32 s19, s17, 1
	s_sub_i32 s18, s4, s14
	s_cmp_ge_u32 s4, s14
	s_cselect_b32 s17, s19, s17
	s_cselect_b32 s4, s18, s4
	s_add_i32 s18, s17, 1
	s_cmp_ge_u32 s4, s14
	s_cselect_b32 s4, s18, s17
	s_xor_b32 s4, s4, s16
	s_sub_i32 s14, s4, s16
	s_mul_i32 s4, s14, s15
	s_sub_i32 s2, s2, s4
	s_add_i32 s16, s2, s5
	s_ashr_i32 s17, s16, 31
	s_lshl_b64 s[4:5], s[16:17], 2
	s_add_u32 s4, s43, s4
	s_addc_u32 s5, s44, s5
	s_load_dword s53, s[4:5], 0x0
	s_waitcnt lgkmcnt(0)

.LBB0_1481:
	s_add_i32 s45, s45, 1
	s_mul_i32 s4, s45, s46
	s_mul_hi_u32 s5, s45, s33
	s_add_i32 s5, s5, s4
	s_mul_i32 s4, s45, s33
	s_add_u32 s4, s4, s87
	s_addc_u32 s5, s5, s47
	v_cmp_ge_i64_e32 vcc, s[4:5], v[128:129]
	v_cmp_lt_i64_e64 s[6:7], s[4:5], v[128:129]
	s_cbranch_vccnz .LBB0_1483
	s_ashr_i32 s5, s4, 31
	s_lshr_b32 s5, s5, 29
	s_add_i32 s5, s4, s5
	s_ashr_i32 s18, s5, 3
	s_and_b32 s5, s5, -8
	s_sub_i32 s4, s4, s5
	s_lshr_b32 s5, s4, 31
	s_add_i32 s5, s3, s5
	s_mul_i32 s4, s5, s4
	s_add_i32 s4, s4, s18
	s_ashr_i32 s5, s4, 31
	s_lshr_b32 s5, s5, 26
	s_add_i32 s5, s4, s5
	s_ashr_i32 s18, s5, 6
	s_lshl_b32 s18, s18, 3
	s_sub_i32 s19, s3, s18
	s_min_i32 s19, s19, 8
	s_abs_i32 s20, s19
	v_cvt_f32_u32_e32 v0, s20
	s_sub_i32 s23, 0, s20
	s_andn2_b32 s5, s5, 63
	s_sub_i32 s4, s4, s5
	v_rcp_iflag_f32_e32 v0, v0
	s_abs_i32 s5, s4
	s_xor_b32 s21, s4, s19
	s_ashr_i32 s21, s21, 31
	v_mul_f32_e32 v0, 0x4f7ffffe, v0
	v_cvt_u32_f32_e32 v0, v0
	s_nop 0
	v_readfirstlane_b32 s26, v0
	s_mul_i32 s23, s23, s26
	s_mul_hi_u32 s23, s26, s23
	s_add_i32 s26, s26, s23
	s_mul_hi_u32 s23, s5, s26
	s_mul_i32 s26, s23, s20
	s_sub_i32 s5, s5, s26
	s_add_i32 s27, s23, 1
	s_sub_i32 s26, s5, s20
	s_cmp_ge_u32 s5, s20
	s_cselect_b32 s23, s27, s23
	s_cselect_b32 s5, s26, s5
	s_add_i32 s26, s23, 1
	s_cmp_ge_u32 s5, s20
	s_cselect_b32 s5, s26, s23
	s_xor_b32 s5, s5, s21
	s_sub_i32 s50, s5, s21
	s_mul_i32 s5, s50, s19
	s_sub_i32 s4, s4, s5
	s_add_i32 s18, s4, s18
	s_ashr_i32 s19, s18, 31
	s_lshl_b64 s[4:5], s[18:19], 2
	s_add_u32 s4, s38, s4
	s_addc_u32 s5, s39, s5
	s_load_dword s19, s[4:5], 0x0
	s_waitcnt lgkmcnt(0)
